# phase 3: first-half stores issued two per MFMA step over the first four steps of the second half
# speedup vs baseline: 1.0028x; 1.0028x over previous
.LBB1_4:
	s_or_b64 exec, exec, s[4:5]
	v_lshl_or_b32 v4, v27, 1, v96
	v_lshl_or_b32 v3, v4, 7, v3
	v_or_b32_e32 v5, 0x23600, v3
	v_or_b32_e32 v3, 0x23640, v3
	s_waitcnt lgkmcnt(0)
	s_barrier
	ds_read_b32 v5, v5
	ds_read_b32 v3, v3
	v_mad_u32_u24 v4, v4, s7, v13
	v_lshl_add_u32 v4, v119, 4, v4
	v_or_b32_e32 v6, 0x20000, v4
	ds_read_b128 v[16:19], v6
	s_waitcnt lgkmcnt(1)
	v_add_f32_e32 v3, v5, v3
	v_add_u32_e32 v5, 0x20020, v4
	v_add_u32_e32 v6, 0x20040, v4
	ds_read_b128 v[112:115], v5
	ds_read_b128 v[108:111], v6
	v_add_u32_e32 v5, 0x20060, v4
	v_add_u32_e32 v6, 0x20080, v4
	v_lshlrev_b32_e32 v7, 1, v101
	ds_read_b128 v[104:107], v5
	ds_read_b128 v[96:99], v6
	v_lshrrev_b32_e32 v5, 2, v100
	v_or_b32_e32 v6, v28, v125
	v_and_b32_e32 v7, 2, v7
	v_bfe_u32 v8, v0, 1, 1
	v_and_b32_e32 v164, 8, v121
	v_bfe_i32 v9, v0, 7, 1
	v_or3_b32 v8, v8, v7, v164
	v_and_b32_e32 v0, 12, v0
	v_add_lshl_u32 v10, v6, v5, 8
	v_or_b32_e32 v5, v6, v5
	v_and_b32_e32 v9, 0xc000, v9
	v_lshlrev_b32_e32 v12, 8, v5
	v_bitop3_b32 v5, v0, v8, v124 bitop3:0x36
	v_lshl_or_b32 v13, v5, 4, v9
	v_bitop3_b32 v6, v0, v8, v2 bitop3:0x36
	v_or_b32_e32 v15, 0x1000, v12
	v_lshl_or_b32 v14, v6, 4, v9
	v_add_u32_e32 v7, v13, v15
	v_or_b32_e32 v24, 0x1400, v12
	v_or_b32_e32 v20, v7, v1
	v_add_u32_e32 v7, v14, v24
	v_add_u32_e32 v25, 0x2000, v10
	v_add_u32_e32 v5, v13, v12
	v_add_u32_e32 v6, v14, v12
	v_or_b32_e32 v22, v7, v1
	v_add_u32_e32 v7, v13, v25
	v_add_u32_e32 v150, 0x3000, v10
	v_or_b32_e32 v8, 4, v8
	v_add_u32_e32 v4, 0x200a0, v4
	v_or_b32_e32 v5, v5, v1
	v_or_b32_e32 v6, v6, v1
	v_or_b32_e32 v27, v7, v1
	v_add_u32_e32 v31, v13, v150
	v_add_u32_e32 v151, 0x3400, v10
	v_bitop3_b32 v124, v0, v8, v124 bitop3:0x36
	v_bitop3_b32 v0, v0, v8, v2 bitop3:0x36
	ds_read_b128 v[100:103], v4
	ds_read_b64_tr_b16 v[4:5], v5
	ds_read_b64_tr_b16 v[6:7], v6 offset:1024
	ds_read_b64_tr_b16 v[20:21], v20
	ds_read_b64_tr_b16 v[22:23], v22
	ds_read_b64_tr_b16 v[28:29], v27
	v_add_u32_e32 v27, 0x2400, v10
	v_or_b32_e32 v128, v31, v1
	v_add_u32_e32 v31, v14, v151
	v_add_u32_e32 v152, 0x4000, v10
	v_add_u32_e32 v158, 0x4400, v10
	v_lshl_or_b32 v124, v124, 4, v9
	v_lshl_or_b32 v0, v0, 4, v9
	v_add_u32_e32 v11, 0x5000, v10
	v_add_u32_e32 v30, v14, v27
	v_or_b32_e32 v130, v31, v1
	v_add_u32_e32 v31, v13, v152
	v_add_u32_e32 v134, v14, v158
	v_add_u32_e32 v10, 0x5400, v10
	v_add_u32_e32 v135, v124, v12
	v_add_u32_e32 v2, v0, v12
	v_add_u32_e32 v8, v124, v15
	v_or_b32_e32 v30, v30, v1
	v_or_b32_e32 v132, v31, v1
	v_or_b32_e32 v134, v134, v1
	v_add_u32_e32 v13, v13, v11
	v_add_u32_e32 v14, v14, v10
	v_or_b32_e32 v140, v135, v1
	v_or_b32_e32 v2, v2, v1
	v_or_b32_e32 v8, v8, v1
	v_add_u32_e32 v9, v0, v24
	v_add_u32_e32 v12, v124, v25
	ds_read_b64_tr_b16 v[30:31], v30
	ds_read_b64_tr_b16 v[128:129], v128
	ds_read_b64_tr_b16 v[130:131], v130
	ds_read_b64_tr_b16 v[132:133], v132
	v_or_b32_e32 v13, v13, v1
	v_or_b32_e32 v14, v14, v1
	ds_read_b64_tr_b16 v[134:135], v134
	ds_read_b64_tr_b16 v[136:137], v13
	ds_read_b64_tr_b16 v[138:139], v14
	ds_read_b64_tr_b16 v[140:141], v140
	v_or_b32_e32 v9, v9, v1
	v_or_b32_e32 v12, v12, v1
	ds_read_b64_tr_b16 v[142:143], v2 offset:1024
	ds_read_b64_tr_b16 v[144:145], v8
	ds_read_b64_tr_b16 v[146:147], v9
	ds_read_b64_tr_b16 v[148:149], v12
	v_add_u32_e32 v2, v0, v27
	v_add_u32_e32 v8, v124, v150
	v_or_b32_e32 v2, v2, v1
	v_or_b32_e32 v8, v8, v1
	v_add_u32_e32 v9, v0, v151
	v_add_u32_e32 v12, v124, v152
	v_or_b32_e32 v9, v9, v1
	v_or_b32_e32 v12, v12, v1
	ds_read_b64_tr_b16 v[150:151], v2
	ds_read_b64_tr_b16 v[152:153], v8
	ds_read_b64_tr_b16 v[154:155], v9
	ds_read_b64_tr_b16 v[156:157], v12
	v_add_u32_e32 v2, v0, v158
	v_add_u32_e32 v8, v124, v11
	v_add_u32_e32 v0, v0, v10
	v_or_b32_e32 v2, v2, v1
	v_or_b32_e32 v8, v8, v1
	v_or_b32_e32 v0, v0, v1
	v_div_scale_f32 v1, s[8:9], v3, v3, 1.0
	v_rcp_f32_e32 v9, v1
	ds_read_b64_tr_b16 v[158:159], v2
	ds_read_b64_tr_b16 v[160:161], v8
	ds_read_b64_tr_b16 v[162:163], v0
	s_mov_b32 s4, 0xc000
	s_movk_i32 s5, 0x4000
	v_fma_f32 v0, -v1, v9, 1.0
	v_fmac_f32_e32 v9, v0, v9
	v_div_scale_f32 v0, vcc, 1.0, v3, 1.0
	v_mul_f32_e32 v2, v0, v9
	v_fma_f32 v8, -v1, v2, v0
	v_fmac_f32_e32 v2, v8, v9
	v_fma_f32 v0, -v1, v2, v0
	v_div_fmas_f32 v0, v0, v9, v2
	v_div_fixup_f32 v124, v0, v3, 1.0
	s_waitcnt lgkmcnt(14)
	v_mfma_f32_32x32x16_f16 v[0:15], v[4:7], v[16:19], 0
	s_mov_b32 s7, 0x18000
	v_lshlrev_b32_e32 v172, 2, v126
	v_mov_b32_e32 v173, 0
	v_mfma_f32_32x32x16_f16 v[0:15], v[20:23], v[112:115], v[0:15]
	v_or_b32_e32 v20, v26, v116
	v_and_b32_e32 v21, 0x4000, v118
	v_lshl_or_b32 v20, v20, 8, v21
	v_bitop3_b32 v118, v121, v120, 8 bitop3:0x6c
	v_or3_b32 v121, v20, v125, s7
	v_mfma_f32_32x32x16_f16 v[0:15], v[28:31], v[108:111], v[0:15]
	v_mfma_f32_32x32x16_f16 v[0:15], v[128:131], v[104:107], v[0:15]
	v_mfma_f32_32x32x16_f16 v[0:15], v[132:135], v[96:99], v[0:15]
	s_waitcnt lgkmcnt(12)
	v_mfma_f32_32x32x16_f16 v[0:15], v[136:139], v[100:103], v[0:15]
	s_nop 11
	v_fma_mixlo_f16 v20, v124, v0, 0
	v_mov_b32_e32 v0, v1
	v_mov_b32_e32 v1, v2
	v_pk_mul_f32 v[0:1], v[124:125], v[0:1] op_sel_hi:[0,1]
	v_cvt_pk_f16_f32 v1, v0, v1
	v_pack_b32_f16 v0, v20, v1
	s_waitcnt lgkmcnt(10)
	v_mfma_f32_32x32x16_f16 v[16:31], v[140:143], v[16:19], 0
	v_fma_mixlo_f16 v2, v124, v3, 0
	v_alignbit_b32 v1, v2, v1, 16
	v_lshl_or_b32 v2, v118, 4, v121
	ds_write_b64 v2, v[0:1]
	v_mov_b32_e32 v0, v5
	v_mov_b32_e32 v1, v6
	v_pk_mul_f32 v[0:1], v[124:125], v[0:1] op_sel_hi:[0,1]
	s_waitcnt lgkmcnt(9)
	v_mfma_f32_32x32x16_f16 v[16:31], v[144:147], v[112:115], v[16:31]
	v_fma_mixlo_f16 v2, v124, v4, 0
	v_cvt_pk_f16_f32 v1, v0, v1
	v_pack_b32_f16 v0, v2, v1
	v_fma_mixlo_f16 v2, v124, v7, 0
	v_alignbit_b32 v1, v2, v1, 16
	v_bitop3_b32 v2, v164, v120, 1 bitop3:0x36
	v_lshl_or_b32 v2, v2, 4, v121
	s_waitcnt lgkmcnt(7)
	v_mfma_f32_32x32x16_f16 v[16:31], v[148:151], v[108:111], v[16:31]
	ds_write_b64 v2, v[0:1]
	v_mov_b32_e32 v0, v9
	v_mov_b32_e32 v1, v10
	v_mul_f32_e64 v0, v124, v0
	v_mul_f32_e64 v1, v124, v1
	v_fma_mixlo_f16 v2, v124, v8, 0
	v_cvt_pk_f16_f32 v1, v0, v1
	v_pack_b32_f16 v0, v2, v1
	s_waitcnt lgkmcnt(6)
	v_mfma_f32_32x32x16_f16 v[16:31], v[152:155], v[104:107], v[16:31]
	v_fma_mixlo_f16 v2, v124, v11, 0
	v_alignbit_b32 v1, v2, v1, 16
	v_bitop3_b32 v2, v164, v120, 2 bitop3:0x36
	v_lshl_or_b32 v2, v2, 4, v121
	ds_write_b64 v2, v[0:1]
	v_mov_b32_e32 v0, v13
	v_mov_b32_e32 v1, v14
	s_waitcnt lgkmcnt(5)
	v_mfma_f32_32x32x16_f16 v[16:31], v[156:159], v[96:99], v[16:31]
	v_mul_f32_e64 v0, v124, v0
	v_mul_f32_e64 v1, v124, v1
	v_fma_mixlo_f16 v2, v124, v12, 0
	v_cvt_pk_f16_f32 v1, v0, v1
	v_pack_b32_f16 v0, v2, v1
	v_fma_mixlo_f16 v2, v124, v15, 0
	v_alignbit_b32 v1, v2, v1, 16
	v_bitop3_b32 v2, v164, v120, 3 bitop3:0x36
	s_waitcnt lgkmcnt(3)
	v_mfma_f32_32x32x16_f16 v[16:31], v[160:163], v[100:103], v[16:31]
	v_lshl_or_b32 v2, v2, 4, v121
	ds_write_b64 v2, v[0:1]
	s_nop 9
	v_mov_b32_e32 v0, v17
	v_mov_b32_e32 v1, v18
	v_pk_mul_f32 v[0:1], v[124:125], v[0:1] op_sel_hi:[0,1]
	v_fma_mixlo_f16 v2, v124, v16, 0
	v_cvt_pk_f16_f32 v1, v0, v1
	v_pack_b32_f16 v0, v2, v1
	v_fma_mixlo_f16 v2, v124, v19, 0
	v_alignbit_b32 v1, v2, v1, 16
	v_bitop3_b32 v2, v164, v120, 4 bitop3:0x36
	v_lshl_or_b32 v2, v2, 4, v121
	ds_write_b64 v2, v[0:1]
	v_mov_b32_e32 v0, v21
	v_mov_b32_e32 v1, v22
	v_pk_mul_f32 v[0:1], v[124:125], v[0:1] op_sel_hi:[0,1]
	v_fma_mixlo_f16 v2, v124, v20, 0
	v_cvt_pk_f16_f32 v1, v0, v1
	v_pack_b32_f16 v0, v2, v1
	v_fma_mixlo_f16 v2, v124, v23, 0
	v_alignbit_b32 v1, v2, v1, 16
	v_bitop3_b32 v2, v164, v120, 5 bitop3:0x36
	v_lshl_or_b32 v2, v2, 4, v121
	ds_write_b64 v2, v[0:1]
	v_mov_b32_e32 v0, v25
	v_mov_b32_e32 v1, v26
	v_pk_mul_f32 v[0:1], v[124:125], v[0:1] op_sel_hi:[0,1]
	v_fma_mixlo_f16 v2, v124, v24, 0
	v_cvt_pk_f16_f32 v1, v0, v1
	v_pack_b32_f16 v0, v2, v1
	v_fma_mixlo_f16 v2, v124, v27, 0
	v_alignbit_b32 v1, v2, v1, 16
	v_bitop3_b32 v2, v164, v120, 6 bitop3:0x36
	v_lshl_or_b32 v2, v2, 4, v121
	ds_write_b64 v2, v[0:1]
	v_mov_b32_e32 v0, v29
	v_mov_b32_e32 v1, v30
	v_pk_mul_f32 v[0:1], v[124:125], v[0:1] op_sel_hi:[0,1]
	v_fma_mixlo_f16 v2, v124, v28, 0
	v_cvt_pk_f16_f32 v1, v0, v1
	v_pack_b32_f16 v0, v2, v1
	v_fma_mixlo_f16 v2, v124, v31, 0
	v_alignbit_b32 v1, v2, v1, 16
	v_bitop3_b32 v2, v164, v120, 7 bitop3:0x36
	v_lshl_or_b32 v2, v2, 4, v121
	ds_write_b64 v2, v[0:1]
	v_lshl_add_u64 v[0:1], s[0:1], 0, v[172:173]
	v_lshlrev_b32_e32 v172, 2, v127
	v_lshl_add_u64 v[0:1], v[0:1], 0, v[172:173]
	s_waitcnt lgkmcnt(0)
	s_barrier
	v_and_b32_e32 v245, 15, v116
	v_lshrrev_b32_e32 v246, 4, v116
	v_lshl_or_b32 v246, v119, 1, v246
	v_lshrrev_b32_e32 v250, 5, v126
	v_and_b32_e32 v250, 7, v250
	v_and_b32_e32 v247, 1, v246
	v_lshrrev_b32_e32 v248, 1, v246
	v_xor_b32_e32 v248, v248, v247
	v_lshl_or_b32 v247, v247, 1, v248
	v_and_b32_e32 v248, 3, v245
	v_lshrrev_b32_e32 v249, 2, v245
	v_lshl_or_b32 v248, v248, 2, v249
	v_xor_b32_e32 v247, v247, v248
	v_lshlrev_b32_e32 v240, 8, v245
	v_lshl_or_b32 v240, v247, 4, v240
	v_add_u32_e32 v240, 0x18000, v240
	v_xor_b32_e32 v241, 64, v240
	v_xor_b32_e32 v242, 0x80, v240
	v_xor_b32_e32 v243, 0xc0, v240
	v_lshlrev_b32_e32 v249, 7, v250
	v_lshl_or_b32 v249, v246, 4, v249
	v_and_b32_e32 v249, 0x3f0, v249
	global_load_dwordx4 v[96:99], v249, s[34:35]
	global_load_dwordx4 v[100:103], v249, s[34:35] offset:64
	v_lshlrev_b32_e32 v244, 19, v250
	v_lshl_or_b32 v244, v246, 16, v244
	v_lshl_or_b32 v244, v245, 3, v244
	v_and_b32_e32 v244, 0x3fff78, v244
	s_lshl_b64 s[22:23], s[2:3], 22
	s_add_u32 s22, s22, s30
	s_addc_u32 s23, s23, s31
	s_lshl_b32 s24, s14, 3
	s_add_u32 s22, s22, s24
	s_addc_u32 s23, s23, 0
	ds_read_b128 v[112:115], v240
	ds_read_b128 v[144:147], v240 offset:8192
	ds_read_b128 v[116:119], v241
	ds_read_b128 v[148:151], v241 offset:8192
	ds_read_b128 v[120:123], v242
	ds_read_b128 v[152:155], v242 offset:8192
	ds_read_b128 v[124:127], v243
	ds_read_b128 v[156:159], v243 offset:8192
	ds_read_b128 v[128:131], v240 offset:16384
	ds_read_b128 v[160:163], v240 offset:24576
	ds_read_b128 v[132:135], v241 offset:16384
	ds_read_b128 v[164:167], v241 offset:24576
	ds_read_b128 v[136:139], v242 offset:16384
	ds_read_b128 v[168:171], v242 offset:24576
	ds_read_b128 v[140:143], v243 offset:16384
	ds_read_b128 v[172:175], v243 offset:24576
	s_waitcnt vmcnt(2)
	s_waitcnt lgkmcnt(14)
	v_mfma_f32_16x16x32_f16 v[0:3], v[36:39], v[112:115], 0
	v_mfma_f32_16x16x32_f16 v[4:7], v[36:39], v[144:147], 0
	v_mfma_f32_16x16x32_f16 v[8:11], v[76:79], v[112:115], 0
	v_mfma_f32_16x16x32_f16 v[12:15], v[76:79], v[144:147], 0
	s_waitcnt lgkmcnt(12)
	v_mfma_f32_16x16x32_f16 v[0:3], v[32:35], v[116:119], v[0:3]
	v_mfma_f32_16x16x32_f16 v[4:7], v[32:35], v[148:151], v[4:7]
	v_mfma_f32_16x16x32_f16 v[8:11], v[72:75], v[116:119], v[8:11]
	v_mfma_f32_16x16x32_f16 v[12:15], v[72:75], v[148:151], v[12:15]
	s_waitcnt lgkmcnt(10)
	v_mfma_f32_16x16x32_f16 v[0:3], v[64:67], v[120:123], v[0:3]
	v_mfma_f32_16x16x32_f16 v[4:7], v[64:67], v[152:155], v[4:7]
	v_mfma_f32_16x16x32_f16 v[8:11], v[68:71], v[120:123], v[8:11]
	v_mfma_f32_16x16x32_f16 v[12:15], v[68:71], v[152:155], v[12:15]
	s_waitcnt lgkmcnt(8)
	v_mfma_f32_16x16x32_f16 v[0:3], v[48:51], v[124:127], v[0:3]
	v_mfma_f32_16x16x32_f16 v[4:7], v[48:51], v[156:159], v[4:7]
	v_mfma_f32_16x16x32_f16 v[8:11], v[52:55], v[124:127], v[8:11]
	v_mfma_f32_16x16x32_f16 v[12:15], v[52:55], v[156:159], v[12:15]
	s_waitcnt lgkmcnt(6)
	v_mfma_f32_16x16x32_f16 v[0:3], v[92:95], v[128:131], v[0:3]
	v_mfma_f32_16x16x32_f16 v[4:7], v[92:95], v[160:163], v[4:7]
	v_mfma_f32_16x16x32_f16 v[8:11], v[60:63], v[128:131], v[8:11]
	v_mfma_f32_16x16x32_f16 v[12:15], v[60:63], v[160:163], v[12:15]
	s_waitcnt lgkmcnt(4)
	v_mfma_f32_16x16x32_f16 v[0:3], v[84:87], v[132:135], v[0:3]
	v_mfma_f32_16x16x32_f16 v[4:7], v[84:87], v[164:167], v[4:7]
	v_mfma_f32_16x16x32_f16 v[8:11], v[56:59], v[132:135], v[8:11]
	v_mfma_f32_16x16x32_f16 v[12:15], v[56:59], v[164:167], v[12:15]
	s_waitcnt lgkmcnt(2)
	v_mfma_f32_16x16x32_f16 v[0:3], v[80:83], v[136:139], v[0:3]
	v_mfma_f32_16x16x32_f16 v[4:7], v[80:83], v[168:171], v[4:7]
	v_mfma_f32_16x16x32_f16 v[8:11], v[44:47], v[136:139], v[8:11]
	v_mfma_f32_16x16x32_f16 v[12:15], v[44:47], v[168:171], v[12:15]
	s_waitcnt lgkmcnt(0)
	v_mfma_f32_16x16x32_f16 v[0:3], v[88:91], v[140:143], v[0:3]
	v_mfma_f32_16x16x32_f16 v[4:7], v[88:91], v[172:175], v[4:7]
	v_mfma_f32_16x16x32_f16 v[8:11], v[40:43], v[140:143], v[8:11]
	v_mfma_f32_16x16x32_f16 v[12:15], v[40:43], v[172:175], v[12:15]
	ds_read_b128 v[176:179], v240 offset:4096
	ds_read_b128 v[208:211], v240 offset:12288
	ds_read_b128 v[180:183], v241 offset:4096
	ds_read_b128 v[212:215], v241 offset:12288
	ds_read_b128 v[184:187], v242 offset:4096
	ds_read_b128 v[216:219], v242 offset:12288
	ds_read_b128 v[188:191], v243 offset:4096
	ds_read_b128 v[220:223], v243 offset:12288
	ds_read_b128 v[192:195], v240 offset:20480
	ds_read_b128 v[224:227], v240 offset:28672
	ds_read_b128 v[196:199], v241 offset:20480
	ds_read_b128 v[228:231], v241 offset:28672
	ds_read_b128 v[200:203], v242 offset:20480
	ds_read_b128 v[232:235], v242 offset:28672
	ds_read_b128 v[204:207], v243 offset:20480
	ds_read_b128 v[236:239], v243 offset:28672
	s_waitcnt vmcnt(0)
	s_waitcnt lgkmcnt(14)
	v_mfma_f32_16x16x32_f16 v[16:19], v[36:39], v[176:179], 0
	v_mfma_f32_16x16x32_f16 v[20:23], v[36:39], v[208:211], 0
	v_mfma_f32_16x16x32_f16 v[24:27], v[76:79], v[176:179], 0
	v_mfma_f32_16x16x32_f16 v[28:31], v[76:79], v[208:211], 0
	s_add_u32 s26, s22, 0x0
	s_addc_u32 s27, s23, 0
	v_add_f32_e32 v104, v0, v96
	v_add_f32_e32 v105, v4, v96
	global_store_dwordx2 v244, v[104:105], s[26:27] nt
	s_add_u32 s26, s22, 0x4000
	s_addc_u32 s27, s23, 0
	v_add_f32_e32 v106, v1, v97
	v_add_f32_e32 v107, v5, v97
	global_store_dwordx2 v244, v[106:107], s[26:27] nt
	s_waitcnt lgkmcnt(12)
	v_mfma_f32_16x16x32_f16 v[16:19], v[32:35], v[180:183], v[16:19]
	v_mfma_f32_16x16x32_f16 v[20:23], v[32:35], v[212:215], v[20:23]
	v_mfma_f32_16x16x32_f16 v[24:27], v[72:75], v[180:183], v[24:27]
	v_mfma_f32_16x16x32_f16 v[28:31], v[72:75], v[212:215], v[28:31]
	s_add_u32 s26, s22, 0x8000
	s_addc_u32 s27, s23, 0
	v_add_f32_e32 v108, v2, v98
	v_add_f32_e32 v109, v6, v98
	global_store_dwordx2 v244, v[108:109], s[26:27] nt
	s_add_u32 s26, s22, 0xc000
	s_addc_u32 s27, s23, 0
	v_add_f32_e32 v110, v3, v99
	v_add_f32_e32 v111, v7, v99
	global_store_dwordx2 v244, v[110:111], s[26:27] nt
	s_waitcnt lgkmcnt(10)
	v_mfma_f32_16x16x32_f16 v[16:19], v[64:67], v[184:187], v[16:19]
	v_mfma_f32_16x16x32_f16 v[20:23], v[64:67], v[216:219], v[20:23]
	v_mfma_f32_16x16x32_f16 v[24:27], v[68:71], v[184:187], v[24:27]
	v_mfma_f32_16x16x32_f16 v[28:31], v[68:71], v[216:219], v[28:31]
	s_add_u32 s26, s22, 0x40000
	s_addc_u32 s27, s23, 0
	v_add_f32_e32 v104, v8, v100
	v_add_f32_e32 v105, v12, v100
	global_store_dwordx2 v244, v[104:105], s[26:27] nt
	s_add_u32 s26, s22, 0x44000
	s_addc_u32 s27, s23, 0
	v_add_f32_e32 v106, v9, v101
	v_add_f32_e32 v107, v13, v101
	global_store_dwordx2 v244, v[106:107], s[26:27] nt
	s_waitcnt lgkmcnt(8)
	v_mfma_f32_16x16x32_f16 v[16:19], v[48:51], v[188:191], v[16:19]
	v_mfma_f32_16x16x32_f16 v[20:23], v[48:51], v[220:223], v[20:23]
	v_mfma_f32_16x16x32_f16 v[24:27], v[52:55], v[188:191], v[24:27]
	v_mfma_f32_16x16x32_f16 v[28:31], v[52:55], v[220:223], v[28:31]
	s_add_u32 s26, s22, 0x48000
	s_addc_u32 s27, s23, 0
	v_add_f32_e32 v108, v10, v102
	v_add_f32_e32 v109, v14, v102
	global_store_dwordx2 v244, v[108:109], s[26:27] nt
	s_add_u32 s26, s22, 0x4c000
	s_addc_u32 s27, s23, 0
	v_add_f32_e32 v110, v11, v103
	v_add_f32_e32 v111, v15, v103
	global_store_dwordx2 v244, v[110:111], s[26:27] nt
	s_waitcnt lgkmcnt(6)
	v_mfma_f32_16x16x32_f16 v[16:19], v[92:95], v[192:195], v[16:19]
	v_mfma_f32_16x16x32_f16 v[20:23], v[92:95], v[224:227], v[20:23]
	v_mfma_f32_16x16x32_f16 v[24:27], v[60:63], v[192:195], v[24:27]
	v_mfma_f32_16x16x32_f16 v[28:31], v[60:63], v[224:227], v[28:31]
	s_waitcnt lgkmcnt(4)
	v_mfma_f32_16x16x32_f16 v[16:19], v[84:87], v[196:199], v[16:19]
	v_mfma_f32_16x16x32_f16 v[20:23], v[84:87], v[228:231], v[20:23]
	v_mfma_f32_16x16x32_f16 v[24:27], v[56:59], v[196:199], v[24:27]
	v_mfma_f32_16x16x32_f16 v[28:31], v[56:59], v[228:231], v[28:31]
	s_waitcnt lgkmcnt(2)
	v_mfma_f32_16x16x32_f16 v[16:19], v[80:83], v[200:203], v[16:19]
	v_mfma_f32_16x16x32_f16 v[20:23], v[80:83], v[232:235], v[20:23]
	v_mfma_f32_16x16x32_f16 v[24:27], v[44:47], v[200:203], v[24:27]
	v_mfma_f32_16x16x32_f16 v[28:31], v[44:47], v[232:235], v[28:31]
	s_waitcnt lgkmcnt(0)
	v_mfma_f32_16x16x32_f16 v[16:19], v[88:91], v[204:207], v[16:19]
	v_mfma_f32_16x16x32_f16 v[20:23], v[88:91], v[236:239], v[20:23]
	v_mfma_f32_16x16x32_f16 v[24:27], v[40:43], v[204:207], v[24:27]
	v_mfma_f32_16x16x32_f16 v[28:31], v[40:43], v[236:239], v[28:31]
	s_nop 7
	s_nop 1
	s_add_u32 s26, s22, 0x0
	s_addc_u32 s27, s23, 0
	v_add_f32_e32 v104, v16, v96
	v_add_f32_e32 v105, v20, v96
	global_store_dwordx2 v244, v[104:105], s[26:27] offset:128 nt
	s_add_u32 s26, s22, 0x4000
	s_addc_u32 s27, s23, 0
	v_add_f32_e32 v106, v17, v97
	v_add_f32_e32 v107, v21, v97
	global_store_dwordx2 v244, v[106:107], s[26:27] offset:128 nt
	s_add_u32 s26, s22, 0x8000
	s_addc_u32 s27, s23, 0
	v_add_f32_e32 v108, v18, v98
	v_add_f32_e32 v109, v22, v98
	global_store_dwordx2 v244, v[108:109], s[26:27] offset:128 nt
	s_add_u32 s26, s22, 0xc000
	s_addc_u32 s27, s23, 0
	v_add_f32_e32 v110, v19, v99
	v_add_f32_e32 v111, v23, v99
	global_store_dwordx2 v244, v[110:111], s[26:27] offset:128 nt
	s_add_u32 s26, s22, 0x40000
	s_addc_u32 s27, s23, 0
	v_add_f32_e32 v104, v24, v100
	v_add_f32_e32 v105, v28, v100
	global_store_dwordx2 v244, v[104:105], s[26:27] offset:128 nt
	s_add_u32 s26, s22, 0x44000
	s_addc_u32 s27, s23, 0
	v_add_f32_e32 v106, v25, v101
	v_add_f32_e32 v107, v29, v101
	global_store_dwordx2 v244, v[106:107], s[26:27] offset:128 nt
	s_add_u32 s26, s22, 0x48000
	s_addc_u32 s27, s23, 0
	v_add_f32_e32 v108, v26, v102
	v_add_f32_e32 v109, v30, v102
	global_store_dwordx2 v244, v[108:109], s[26:27] offset:128 nt
	s_add_u32 s26, s22, 0x4c000
	s_addc_u32 s27, s23, 0
	v_add_f32_e32 v110, v27, v103
	v_add_f32_e32 v111, v31, v103
	global_store_dwordx2 v244, v[110:111], s[26:27] offset:128 nt
	s_endpgm
